# v59 + weight-copy chunks: waves 4-7 start ~2.4us later (s_sleep 80) so the two waves of a SIMD alternate load-wait and transpose/store instead of lockstep
# speedup vs baseline: 1.0062x; 1.0062x over previous
.LBB6_901:
	s_lshl_b32 s84, s0, 3
	s_or_b32 s1, s84, s59
	s_mul_hi_i32 s3, s63, s1
	s_mul_i32 s2, s63, s1
	s_lshr_b64 s[2:3], s[2:3], 9
	s_add_i32 s1, s1, 1
	s_and_b32 s90, s2, 0xffffffe0
	s_mul_hi_i32 s3, s63, s1
	s_mul_i32 s2, s63, s1
	s_lshr_b64 s[2:3], s[2:3], 9
	s_and_b32 s91, s2, 0xffffffe0
	s_bitcmp0_b32 s0, 0
	s_cselect_b64 s[22:23], -1, 0
	s_and_b64 vcc, exec, s[22:23]
	s_cbranch_vccnz .LBB6_1210
	v_readfirstlane_b32 s98, v0
	s_nop 0
	s_bitcmp1_b32 s98, 8
	s_cbranch_scc0 .Ldephase_a
	s_sleep 80
.Ldephase_a:
	v_readlane_b32 s6, v254, 13
	v_readlane_b32 s7, v254, 14
	s_waitcnt vmcnt(0)
	v_mov_b32_e32 v167, v0
	s_max_i32 s64, s90, 0
	v_readfirstlane_b32 s0, v167
	s_ashr_i32 s95, s0, 6
	v_readlane_b32 s0, v254, 60
	s_lshl_b32 s81, s95, 14
	v_readlane_b32 s1, v254, 61
	v_and_b32_e32 v166, 63, v167
	s_add_i32 s94, s81, 0
	s_mov_b64 s[2:3], -1
	s_and_b64 vcc, exec, s[0:1]
	s_cbranch_vccz .LBB6_915
	s_min_i32 s30, s91, 0xdc00
	s_cmp_le_i32 s30, s64
	s_cbranch_scc1 .LBB6_908
	s_sub_i32 s0, s30, s64
	s_mov_b32 s2, 18
	s_cmp_lt_i32 s0, 32
	s_cbranch_scc1 .LBB6_908
	s_add_i32 s31, s95, s64
	s_cmp_ge_i32 s31, s30
	s_cbranch_scc1 .LBB6_908
	s_ashr_i32 s3, s2, 31
	s_lshl_b64 s[0:1], s[2:3], 3
	s_add_u32 s0, s76, s0
	s_addc_u32 s1, s77, s1
	s_load_dwordx2 s[0:1], s[0:1], 0x0
	v_lshrrev_b32_e32 v4, 3, v166
	v_lshlrev_b32_e32 v2, 2, v166
	v_mul_u32_u24_e32 v5, 0x2c00, v4
	v_and_b32_e32 v6, 28, v2
	s_waitcnt lgkmcnt(0)
	s_add_u32 s34, s0, 0x10800000
	v_or_b32_e32 v2, v5, v6
	v_lshl_add_u32 v5, v6, 2, s94
	v_lshlrev_b32_e32 v6, 5, v166
	s_addc_u32 s35, s1, 0
	v_lshrrev_b32_e32 v135, 2, v166
	v_lshlrev_b32_e32 v132, 4, v166
	v_and_b32_e32 v132, 48, v132
	s_add_u32 s36, s6, 0x85280000
	v_mul_u32_u24_e32 v4, 0x84, v4
	v_mul_u32_u24_e32 v6, 0x84, v132
	v_lshlrev_b32_e32 v7, 2, v135
	v_and_b32_e32 v134, 31, v167
	s_addc_u32 s37, s7, 0
	v_lshlrev_b32_e32 v2, 2, v2
	v_add3_u32 v136, s94, v6, v7
	v_mov_b32_e32 v133, v3
	v_add_u32_e32 v137, v5, v4

.LBB6_1307:
	v_readlane_b32 s6, v254, 13
	v_readlane_b32 s7, v254, 14
	s_waitcnt vmcnt(0)
	v_mov_b32_e32 v167, v0
	s_waitcnt lgkmcnt(0)
	s_barrier
	v_readfirstlane_b32 s98, v0
	s_nop 0
	s_bitcmp1_b32 s98, 8
	s_cbranch_scc0 .Ldephase_b
	s_sleep 80
.Ldephase_b:
	s_max_i32 s36, s90, 0
	v_readfirstlane_b32 s0, v167
	s_ashr_i32 s67, s0, 6
	v_readlane_b32 s0, v254, 60
	s_lshl_b32 s81, s67, 14
	v_readlane_b32 s1, v254, 61
	v_and_b32_e32 v166, 63, v167
	s_add_i32 s66, s81, 0
	s_mov_b64 s[2:3], -1
	s_and_b64 vcc, exec, s[0:1]
	s_cbranch_vccz .LBB6_1319
	s_min_i32 s28, s91, 0xdc00
	s_cmp_le_i32 s28, s36
	s_cbranch_scc1 .LBB6_1313
	s_sub_i32 s0, s28, s36
	s_mov_b32 s2, 18
	s_cmp_lt_i32 s0, 32
	s_cbranch_scc1 .LBB6_1313
	s_add_i32 s29, s67, s36
	s_cmp_ge_i32 s29, s28
	s_cbranch_scc1 .LBB6_1313
	s_ashr_i32 s3, s2, 31
	s_lshl_b64 s[0:1], s[2:3], 3
	s_add_u32 s0, s76, s0
	s_addc_u32 s1, s77, s1
	s_load_dwordx2 s[0:1], s[0:1], 0x0
	v_lshrrev_b32_e32 v4, 3, v166
	v_lshlrev_b32_e32 v2, 2, v166
	v_mul_u32_u24_e32 v5, 0x2c00, v4
	v_and_b32_e32 v6, 28, v2
	s_waitcnt lgkmcnt(0)
	s_add_u32 s30, s0, 0x10800000
	v_or_b32_e32 v2, v5, v6
	v_lshl_add_u32 v5, v6, 2, s66
	v_lshlrev_b32_e32 v6, 5, v166
	s_addc_u32 s31, s1, 0
	v_lshrrev_b32_e32 v135, 2, v166
	v_lshlrev_b32_e32 v132, 4, v166
	v_and_b32_e32 v132, 48, v132
	s_add_u32 s34, s6, 0x85280000
	v_mul_u32_u24_e32 v4, 0x84, v4
	v_mul_u32_u24_e32 v6, 0x84, v132
	v_lshlrev_b32_e32 v7, 2, v135
	v_and_b32_e32 v134, 31, v167
	s_addc_u32 s35, s7, 0
	v_lshlrev_b32_e32 v2, 2, v2
	v_add3_u32 v136, s66, v6, v7
	v_mov_b32_e32 v133, v3
	v_add_u32_e32 v137, v5, v4

.LBB6_2087:
	s_mov_b32 s0, s96
	s_cmpk_lt_i32 s0, 0x80
	s_cbranch_scc1 .LBB6_2098
	v_readlane_b32 s2, v254, 13
	v_readlane_b32 s3, v254, 14
	v_mov_b32_e32 v135, v0
	s_waitcnt vmcnt(0) lgkmcnt(0)
	s_barrier
	v_readfirstlane_b32 s98, v0
	s_nop 0
	s_bitcmp1_b32 s98, 8
	s_cbranch_scc0 .Ldephase_c
	s_sleep 80
.Ldephase_c:
	s_mul_i32 s19, s0, 0xa0
	s_add_i32 s18, s19, 0xaa00
	v_readfirstlane_b32 s0, v135
	s_ashr_i32 s17, s0, 6
	s_add_i32 s19, s19, 0xaaa0
	s_lshl_b32 s0, s17, 14
	s_add_i32 s16, s0, 0
	s_max_i32 s0, s18, 0
	s_min_i32 s20, s19, 0xdc00
	s_cmp_le_i32 s20, s0
	v_and_b32_e32 v134, 63, v135
	s_cbranch_scc1 .LBB6_2093
	s_sub_i32 s1, s20, s0
	s_mov_b32 s4, 18
	s_cmp_lt_i32 s1, 32
	s_cbranch_scc1 .LBB6_2093
	s_add_i32 s21, s17, s0
	s_cmp_ge_i32 s21, s20
	s_cbranch_scc1 .LBB6_2093
	s_ashr_i32 s5, s4, 31
	s_lshl_b64 s[0:1], s[4:5], 3
	s_add_u32 s0, s76, s0
	s_addc_u32 s1, s77, s1
	s_load_dwordx2 s[0:1], s[0:1], 0x0
	v_lshrrev_b32_e32 v4, 3, v134
	v_lshlrev_b32_e32 v2, 2, v134
	v_mul_u32_u24_e32 v5, 0x2c00, v4
	v_and_b32_e32 v6, 28, v2
	s_waitcnt lgkmcnt(0)
	s_add_u32 s22, s0, 0x10800000
	v_or_b32_e32 v2, v5, v6
	v_lshl_add_u32 v5, v6, 2, s16
	v_lshlrev_b32_e32 v6, 5, v134
	s_addc_u32 s23, s1, 0
	v_lshrrev_b32_e32 v137, 2, v134
	v_lshlrev_b32_e32 v132, 4, v134
	v_and_b32_e32 v132, 48, v132
	s_add_u32 s24, s2, 0x85280000
	v_mul_u32_u24_e32 v4, 0x84, v4
	v_mul_u32_u24_e32 v6, 0x84, v132
	v_lshlrev_b32_e32 v7, 2, v137
	v_and_b32_e32 v136, 31, v135
	s_addc_u32 s25, s3, 0
	v_lshlrev_b32_e32 v2, 2, v2
	v_add3_u32 v138, s16, v6, v7
	v_mov_b32_e32 v133, v3
	v_add_u32_e32 v139, v5, v4
